# topic loop laid out so every 8-byte instruction (VOP3 fma, DS ops) starts on an 8-byte boundary
# speedup vs baseline: 1.0022x; 1.0022x over previous
.LBB1_53:
	s_or_b64 exec, exec, s[2:3]
	v_add_f32_e32 v130, v130, v14
	v_or_b32_e32 v14, v212, v214
	v_add_f32_e32 v134, v134, v10
	v_add_f32_e32 v10, v110, v50
	v_add_f32_e32 v50, v98, v58
	v_add_f32_e32 v58, v90, v62
	v_add_u32_e32 v62, 0x17080, v14
	v_add_f32_e32 v131, v131, v15
	v_add_f32_e32 v132, v132, v16
	v_add_f32_e32 v133, v133, v17
	v_add_f32_e32 v82, v82, v30
	ds_read_b128 v[14:17], v62
	v_add_f32_e32 v83, v83, v31
	v_add_f32_e32 v84, v84, v32
	v_add_f32_e32 v85, v85, v33
	ds_read_b128 v[30:33], v62 offset:32
	v_add_f32_e32 v2, v142, v2
	v_add_f32_e32 v138, v138, v6
	v_add_f32_e32 v6, v126, v34
	v_add_f32_e32 v34, v122, v38
	v_add_f32_e32 v38, v118, v42
	v_add_f32_e32 v114, v114, v46
	v_add_f32_e32 v42, v106, v54
	v_add_f32_e32 v18, v102, v18
	v_add_f32_e32 v46, v94, v22
	v_add_f32_e32 v141, v141, v9
	v_add_f32_e32 v135, v135, v11
	v_add_f32_e32 v136, v136, v12
	v_add_f32_e32 v137, v137, v13
	v_add_f32_e32 v9, v129, v37
	v_add_f32_e32 v37, v125, v41
	v_add_f32_e32 v41, v121, v45
	v_add_f32_e32 v115, v115, v47
	v_add_f32_e32 v116, v116, v48
	v_add_f32_e32 v117, v117, v49
	v_add_f32_e32 v11, v111, v51
	v_add_f32_e32 v12, v112, v52
	v_add_f32_e32 v13, v113, v53
	v_add_f32_e32 v45, v109, v57
	v_add_f32_e32 v51, v99, v59
	v_add_f32_e32 v52, v100, v60
	v_add_f32_e32 v53, v101, v61
	v_add_f32_e32 v59, v91, v63
	v_add_f32_e32 v60, v92, v64
	v_add_f32_e32 v61, v93, v65
	v_add_f32_e32 v57, v86, v26
	s_waitcnt lgkmcnt(1)
	v_add_f32_e32 v2, v14, v2
	v_add_f32_e32 v6, v14, v6
	v_add_f32_e32 v10, v14, v10
	v_add_f32_e32 v14, v14, v18
	s_waitcnt lgkmcnt(0)
	v_add_f32_e32 v18, v30, v138
	v_add_f32_e32 v22, v30, v34
	v_add_f32_e32 v26, v30, v42
	v_add_f32_e32 v30, v30, v46
	ds_read_b128 v[46:49], v62 offset:64
	ds_read_b128 v[62:65], v62 offset:96
	v_add_f32_e32 v3, v143, v3
	v_add_f32_e32 v4, v144, v4
	v_add_f32_e32 v5, v145, v5
	v_add_f32_e32 v139, v139, v7
	v_add_f32_e32 v140, v140, v8
	v_add_f32_e32 v7, v127, v35
	v_add_f32_e32 v8, v128, v36
	v_add_f32_e32 v35, v123, v39
	v_add_f32_e32 v36, v124, v40
	v_add_f32_e32 v39, v119, v43
	v_add_f32_e32 v40, v120, v44
	v_add_f32_e32 v43, v107, v55
	v_add_f32_e32 v44, v108, v56
	v_add_f32_e32 v19, v103, v19
	v_add_f32_e32 v20, v104, v20
	v_add_f32_e32 v21, v105, v21
	v_add_f32_e32 v54, v95, v23
	v_add_f32_e32 v55, v96, v24
	v_add_f32_e32 v56, v97, v25
	v_add_f32_e32 v86, v87, v27
	v_add_f32_e32 v87, v88, v28
	v_add_f32_e32 v88, v89, v29
	v_add_f32_e32 v3, v15, v3
	v_add_f32_e32 v4, v16, v4
	v_add_f32_e32 v5, v17, v5
	v_add_f32_e32 v7, v15, v7
	v_add_f32_e32 v8, v16, v8
	v_add_f32_e32 v9, v17, v9
	v_add_f32_e32 v11, v15, v11
	v_add_f32_e32 v12, v16, v12
	v_add_f32_e32 v13, v17, v13
	v_add_f32_e32 v15, v15, v19
	v_add_f32_e32 v16, v16, v20
	v_add_f32_e32 v17, v17, v21
	v_add_f32_e32 v19, v31, v139
	v_add_f32_e32 v20, v32, v140
	v_add_f32_e32 v21, v33, v141
	v_add_f32_e32 v23, v31, v35
	v_add_f32_e32 v24, v32, v36
	v_add_f32_e32 v25, v33, v37
	v_add_f32_e32 v27, v31, v43
	v_add_f32_e32 v28, v32, v44
	v_add_f32_e32 v29, v33, v45
	v_add_f32_e32 v31, v31, v54
	v_add_f32_e32 v32, v32, v55
	v_add_f32_e32 v33, v33, v56
	s_waitcnt lgkmcnt(1)
	v_add_f32_e32 v34, v46, v134
	v_add_f32_e32 v38, v46, v38
	v_add_f32_e32 v42, v46, v50
	v_add_f32_e32 v43, v47, v51
	v_add_f32_e32 v44, v48, v52
	v_add_f32_e32 v45, v49, v53
	v_add_f32_e32 v46, v46, v57
	s_waitcnt lgkmcnt(0)
	v_add_f32_e32 v50, v62, v130
	v_add_f32_e32 v51, v63, v131
	v_add_f32_e32 v52, v64, v132
	v_add_f32_e32 v53, v65, v133
	v_add_f32_e32 v54, v62, v114
	v_add_f32_e32 v55, v63, v115
	v_add_f32_e32 v56, v64, v116
	v_add_f32_e32 v57, v65, v117
	v_add_f32_e32 v58, v62, v58
	v_add_f32_e32 v59, v63, v59
	v_add_f32_e32 v60, v64, v60
	v_add_f32_e32 v61, v65, v61
	v_add_f32_e32 v62, v62, v82
	v_add_f32_e32 v63, v63, v83
	v_add_f32_e32 v64, v64, v84
	v_add_f32_e32 v65, v65, v85
	s_waitcnt vmcnt(3)
	v_fma_f32 v82, v66, v2, 0
	v_fma_f32 v83, v66, v6, 0
	v_fma_f32 v84, v66, v10, 0
	v_fma_f32 v85, v66, v14, 0
	v_fmac_f32_e32 v82, v67, v3
	v_fmac_f32_e32 v83, v67, v7
	v_fmac_f32_e32 v84, v67, v11
	v_fmac_f32_e32 v85, v67, v15
	v_fmac_f32_e32 v82, v68, v4
	v_fmac_f32_e32 v83, v68, v8
	v_fmac_f32_e32 v84, v68, v12
	v_fmac_f32_e32 v85, v68, v16
	v_fmac_f32_e32 v82, v69, v5
	v_fmac_f32_e32 v83, v69, v9
	v_fmac_f32_e32 v84, v69, v13
	v_fmac_f32_e32 v85, v69, v17
	s_waitcnt vmcnt(2)
	v_fmac_f32_e32 v82, v70, v18
	v_fmac_f32_e32 v83, v70, v22
	v_fmac_f32_e32 v84, v70, v26
	v_fmac_f32_e32 v85, v70, v30
	v_fmac_f32_e32 v82, v71, v19
	v_fmac_f32_e32 v83, v71, v23
	v_fmac_f32_e32 v84, v71, v27
	v_fmac_f32_e32 v85, v71, v31
	v_fmac_f32_e32 v82, v72, v20
	v_fmac_f32_e32 v83, v72, v24
	v_fmac_f32_e32 v84, v72, v28
	v_fmac_f32_e32 v85, v72, v32
	v_fmac_f32_e32 v82, v73, v21
	v_fmac_f32_e32 v83, v73, v25
	v_fmac_f32_e32 v84, v73, v29
	v_fmac_f32_e32 v85, v73, v33
	v_add_f32_e32 v35, v47, v135
	v_add_f32_e32 v39, v47, v39
	v_add_f32_e32 v47, v47, v86
	s_waitcnt vmcnt(1)
	v_fmac_f32_e32 v82, v74, v34
	v_fmac_f32_e32 v83, v74, v38
	v_fmac_f32_e32 v84, v74, v42
	v_fmac_f32_e32 v85, v74, v46
	v_add_f32_e32 v36, v48, v136
	v_add_f32_e32 v40, v48, v40
	v_add_f32_e32 v48, v48, v87
	v_fmac_f32_e32 v82, v75, v35
	v_fmac_f32_e32 v83, v75, v39
	v_fmac_f32_e32 v84, v75, v43
	v_fmac_f32_e32 v85, v75, v47
	v_add_f32_e32 v37, v49, v137
	v_add_f32_e32 v41, v49, v41
	v_add_f32_e32 v49, v49, v88
	v_fmac_f32_e32 v82, v76, v36
	v_fmac_f32_e32 v83, v76, v40
	v_fmac_f32_e32 v84, v76, v44
	v_fmac_f32_e32 v85, v76, v48
	v_fmac_f32_e32 v82, v77, v37
	v_fmac_f32_e32 v83, v77, v41
	v_fmac_f32_e32 v84, v77, v45
	v_fmac_f32_e32 v85, v77, v49
	s_waitcnt vmcnt(0)
	v_fmac_f32_e32 v82, v78, v50
	v_fmac_f32_e32 v83, v78, v54
	v_fmac_f32_e32 v84, v78, v58
	v_fmac_f32_e32 v85, v78, v62
	v_mul_u32_u24_e32 v87, 10, v225
	v_lshlrev_b32_e32 v1, 9, v1
	v_fmac_f32_e32 v82, v79, v51
	v_fmac_f32_e32 v83, v79, v55
	v_fmac_f32_e32 v84, v79, v59
	v_fmac_f32_e32 v85, v79, v63
	v_lshlrev_b32_e32 v86, 9, v87
	v_lshl_or_b32 v1, v87, 12, v1
	v_lshlrev_b32_e32 v87, 10, v224
	v_fmac_f32_e32 v82, v80, v52
	v_fmac_f32_e32 v83, v80, v56
	v_fmac_f32_e32 v84, v80, v60
	v_fmac_f32_e32 v85, v80, v64
	v_or3_b32 v1, v87, v1, v211
	v_fmac_f32_e32 v82, v81, v53
	v_fmac_f32_e32 v83, v81, v57
	v_fmac_f32_e32 v84, v81, v61
	v_fmac_f32_e32 v85, v81, v65
	v_or3_b32 v86, v86, v212, v214
	v_add_u32_e32 v1, 0x2800, v1
	s_mov_b32 s0, 0
	v_mul_f32_e32 v66, 0.5, v66
	v_mul_f32_e32 v67, 0.5, v67
	v_mul_f32_e32 v68, 0.5, v68
	v_mul_f32_e32 v69, 0.5, v69
	v_mul_f32_e32 v70, 0.5, v70
	v_mul_f32_e32 v71, 0.5, v71
	v_mul_f32_e32 v72, 0.5, v72
	v_mul_f32_e32 v73, 0.5, v73
	v_mul_f32_e32 v74, 0.5, v74
	v_mul_f32_e32 v75, 0.5, v75
	v_mul_f32_e32 v76, 0.5, v76
	v_mul_f32_e32 v77, 0.5, v77
	v_mul_f32_e32 v78, 0.5, v78
	v_mul_f32_e32 v79, 0.5, v79
	v_mul_f32_e32 v80, 0.5, v80
	v_mul_f32_e32 v81, 0.5, v81
	v_mul_f32_e32 v82, 0.5, v82
	v_mul_f32_e32 v83, 0.5, v83
	v_mul_f32_e32 v84, 0.5, v84
	v_mul_f32_e32 v85, 0.5, v85
	.p2align	3
	v_add_u32_e32 v152, s0, v86
	s_addk_i32 s0, 0x200
	ds_read_b128 v[88:91], v152
	ds_read_b128 v[92:95], v152 offset:32
	ds_read_b128 v[96:99], v152 offset:64
	ds_read_b128 v[100:103], v152 offset:96
.Ltopic_loop:
	v_add_u32_e32 v152, s0, v86
	s_addk_i32 s0, 0x200
	ds_read_b128 v[136:139], v152
	ds_read_b128 v[140:143], v152 offset:32
	ds_read_b128 v[144:147], v152 offset:64
	ds_read_b128 v[148:151], v152 offset:96
	s_waitcnt lgkmcnt(4)
	v_add_f32_e32 v104, v2, v88
	v_add_f32_e32 v108, v6, v88
	v_add_f32_e32 v112, v10, v88
	v_add_f32_e32 v116, v14, v88
	v_add_f32_e32 v105, v3, v89
	v_add_f32_e32 v109, v7, v89
	v_add_f32_e32 v113, v11, v89
	v_add_f32_e32 v117, v15, v89
	v_add_f32_e32 v106, v4, v90
	v_add_f32_e32 v110, v8, v90
	v_add_f32_e32 v114, v12, v90
	v_add_f32_e32 v118, v16, v90
	v_add_f32_e32 v107, v5, v91
	v_add_f32_e32 v111, v9, v91
	v_add_f32_e32 v115, v13, v91
	v_add_f32_e32 v119, v17, v91
	v_mul_f32_e32 v87, v66, v88
	v_fmac_f32_e32 v87, v67, v89
	s_nop 0
	v_fma_f32 v160, v66, |v104|, v82
	v_fma_f32 v161, v66, |v108|, v83
	v_fma_f32 v162, v66, |v112|, v84
	v_fma_f32 v163, v66, |v116|, v85
	v_fma_f32 v160, v67, |v105|, v160
	v_fma_f32 v161, v67, |v109|, v161
	v_fma_f32 v162, v67, |v113|, v162
	v_fma_f32 v163, v67, |v117|, v163
	v_fmac_f32_e32 v87, v68, v90
	v_fmac_f32_e32 v87, v69, v91
	v_fma_f32 v160, v68, |v106|, v160
	v_fma_f32 v161, v68, |v110|, v161
	v_fma_f32 v162, v68, |v114|, v162
	v_fma_f32 v163, v68, |v118|, v163
	v_fma_f32 v160, v69, |v107|, v160
	v_fma_f32 v161, v69, |v111|, v161
	v_fma_f32 v162, v69, |v115|, v162
	v_fma_f32 v163, v69, |v119|, v163
	v_add_f32_e32 v120, v18, v92
	v_add_f32_e32 v124, v22, v92
	v_add_f32_e32 v128, v26, v92
	v_add_f32_e32 v132, v30, v92
	v_add_f32_e32 v121, v19, v93
	v_add_f32_e32 v125, v23, v93
	v_add_f32_e32 v129, v27, v93
	v_add_f32_e32 v133, v31, v93
	v_add_f32_e32 v122, v20, v94
	v_add_f32_e32 v126, v24, v94
	v_add_f32_e32 v130, v28, v94
	v_add_f32_e32 v134, v32, v94
	v_add_f32_e32 v123, v21, v95
	v_add_f32_e32 v127, v25, v95
	v_add_f32_e32 v131, v29, v95
	v_add_f32_e32 v135, v33, v95
	v_fmac_f32_e32 v87, v70, v92
	v_fmac_f32_e32 v87, v71, v93
	v_fma_f32 v160, v70, |v120|, v160
	v_fma_f32 v161, v70, |v124|, v161
	v_fma_f32 v162, v70, |v128|, v162
	v_fma_f32 v163, v70, |v132|, v163
	v_fma_f32 v160, v71, |v121|, v160
	v_fma_f32 v161, v71, |v125|, v161
	v_fma_f32 v162, v71, |v129|, v162
	v_fma_f32 v163, v71, |v133|, v163
	v_fmac_f32_e32 v87, v72, v94
	v_fmac_f32_e32 v87, v73, v95
	v_fma_f32 v160, v72, |v122|, v160
	v_fma_f32 v161, v72, |v126|, v161
	v_fma_f32 v162, v72, |v130|, v162
	v_fma_f32 v163, v72, |v134|, v163
	v_fma_f32 v160, v73, |v123|, v160
	v_fma_f32 v161, v73, |v127|, v161
	v_fma_f32 v162, v73, |v131|, v162
	v_fma_f32 v163, v73, |v135|, v163
	v_add_f32_e32 v104, v34, v96
	v_add_f32_e32 v108, v38, v96
	v_add_f32_e32 v112, v42, v96
	v_add_f32_e32 v116, v46, v96
	v_add_f32_e32 v105, v35, v97
	v_add_f32_e32 v109, v39, v97
	v_add_f32_e32 v113, v43, v97
	v_add_f32_e32 v117, v47, v97
	v_add_f32_e32 v106, v36, v98
	v_add_f32_e32 v110, v40, v98
	v_add_f32_e32 v114, v44, v98
	v_add_f32_e32 v118, v48, v98
	v_add_f32_e32 v107, v37, v99
	v_add_f32_e32 v111, v41, v99
	v_add_f32_e32 v115, v45, v99
	v_add_f32_e32 v119, v49, v99
	v_fmac_f32_e32 v87, v74, v96
	v_fmac_f32_e32 v87, v75, v97
	v_fma_f32 v160, v74, |v104|, v160
	v_fma_f32 v161, v74, |v108|, v161
	v_fma_f32 v162, v74, |v112|, v162
	v_fma_f32 v163, v74, |v116|, v163
	v_fma_f32 v160, v75, |v105|, v160
	v_fma_f32 v161, v75, |v109|, v161
	v_fma_f32 v162, v75, |v113|, v162
	v_fma_f32 v163, v75, |v117|, v163
	v_fmac_f32_e32 v87, v76, v98
	v_fmac_f32_e32 v87, v77, v99
	v_fma_f32 v160, v76, |v106|, v160
	v_fma_f32 v161, v76, |v110|, v161
	v_fma_f32 v162, v76, |v114|, v162
	v_fma_f32 v163, v76, |v118|, v163
	v_fma_f32 v160, v77, |v107|, v160
	v_fma_f32 v161, v77, |v111|, v161
	v_fma_f32 v162, v77, |v115|, v162
	v_fma_f32 v163, v77, |v119|, v163
	v_add_f32_e32 v120, v50, v100
	v_add_f32_e32 v124, v54, v100
	v_add_f32_e32 v128, v58, v100
	v_add_f32_e32 v132, v62, v100
	v_add_f32_e32 v121, v51, v101
	v_add_f32_e32 v125, v55, v101
	v_add_f32_e32 v129, v59, v101
	v_add_f32_e32 v133, v63, v101
	v_add_f32_e32 v122, v52, v102
	v_add_f32_e32 v126, v56, v102
	v_add_f32_e32 v130, v60, v102
	v_add_f32_e32 v134, v64, v102
	v_add_f32_e32 v123, v53, v103
	v_add_f32_e32 v127, v57, v103
	v_add_f32_e32 v131, v61, v103
	v_add_f32_e32 v135, v65, v103
	v_fmac_f32_e32 v87, v78, v100
	v_fmac_f32_e32 v87, v79, v101
	v_fma_f32 v160, v78, |v120|, v160
	v_fma_f32 v161, v78, |v124|, v161
	v_fma_f32 v162, v78, |v128|, v162
	v_fma_f32 v163, v78, |v132|, v163
	v_fma_f32 v160, v79, |v121|, v160
	v_fma_f32 v161, v79, |v125|, v161
	v_fma_f32 v162, v79, |v129|, v162
	v_fma_f32 v163, v79, |v133|, v163
	v_fmac_f32_e32 v87, v80, v102
	v_fmac_f32_e32 v87, v81, v103
	v_fma_f32 v160, v80, |v122|, v160
	v_fma_f32 v161, v80, |v126|, v161
	v_fma_f32 v162, v80, |v130|, v162
	v_fma_f32 v163, v80, |v134|, v163
	v_fma_f32 v160, v81, |v123|, v160
	v_fma_f32 v161, v81, |v127|, v161
	v_fma_f32 v162, v81, |v131|, v162
	v_fma_f32 v163, v81, |v135|, v163
	v_add_f32_e32 v160, v160, v87
	v_add_f32_e32 v161, v161, v87
	v_add_f32_e32 v162, v162, v87
	v_add_f32_e32 v163, v163, v87
	ds_write2_b32 v1, v160, v161 offset1:32
	ds_write2_b32 v1, v162, v163 offset0:64 offset1:96
	v_add_u32_e32 v1, 0x1000, v1
	v_add_u32_e32 v152, s0, v86
	s_addk_i32 s0, 0x200
	ds_read_b128 v[88:91], v152
	ds_read_b128 v[92:95], v152 offset:32
	ds_read_b128 v[96:99], v152 offset:64
	ds_read_b128 v[100:103], v152 offset:96
	s_waitcnt lgkmcnt(4)
	v_add_f32_e32 v104, v2, v136
	v_add_f32_e32 v108, v6, v136
	v_add_f32_e32 v112, v10, v136
	v_add_f32_e32 v116, v14, v136
	v_add_f32_e32 v105, v3, v137
	v_add_f32_e32 v109, v7, v137
	v_add_f32_e32 v113, v11, v137
	v_add_f32_e32 v117, v15, v137
	v_add_f32_e32 v106, v4, v138
	v_add_f32_e32 v110, v8, v138
	v_add_f32_e32 v114, v12, v138
	v_add_f32_e32 v118, v16, v138
	v_add_f32_e32 v107, v5, v139
	v_add_f32_e32 v111, v9, v139
	v_add_f32_e32 v115, v13, v139
	v_add_f32_e32 v119, v17, v139
	v_mul_f32_e32 v87, v66, v136
	v_fmac_f32_e32 v87, v67, v137
	s_nop 0
	v_fma_f32 v160, v66, |v104|, v82
	v_fma_f32 v161, v66, |v108|, v83
	v_fma_f32 v162, v66, |v112|, v84
	v_fma_f32 v163, v66, |v116|, v85
	v_fma_f32 v160, v67, |v105|, v160
	v_fma_f32 v161, v67, |v109|, v161
	v_fma_f32 v162, v67, |v113|, v162
	v_fma_f32 v163, v67, |v117|, v163
	v_fmac_f32_e32 v87, v68, v138
	v_fmac_f32_e32 v87, v69, v139
	v_fma_f32 v160, v68, |v106|, v160
	v_fma_f32 v161, v68, |v110|, v161
	v_fma_f32 v162, v68, |v114|, v162
	v_fma_f32 v163, v68, |v118|, v163
	v_fma_f32 v160, v69, |v107|, v160
	v_fma_f32 v161, v69, |v111|, v161
	v_fma_f32 v162, v69, |v115|, v162
	v_fma_f32 v163, v69, |v119|, v163
	v_add_f32_e32 v120, v18, v140
	v_add_f32_e32 v124, v22, v140
	v_add_f32_e32 v128, v26, v140
	v_add_f32_e32 v132, v30, v140
	v_add_f32_e32 v121, v19, v141
	v_add_f32_e32 v125, v23, v141
	v_add_f32_e32 v129, v27, v141
	v_add_f32_e32 v133, v31, v141
	v_add_f32_e32 v122, v20, v142
	v_add_f32_e32 v126, v24, v142
	v_add_f32_e32 v130, v28, v142
	v_add_f32_e32 v134, v32, v142
	v_add_f32_e32 v123, v21, v143
	v_add_f32_e32 v127, v25, v143
	v_add_f32_e32 v131, v29, v143
	v_add_f32_e32 v135, v33, v143
	v_fmac_f32_e32 v87, v70, v140
	v_fmac_f32_e32 v87, v71, v141
	v_fma_f32 v160, v70, |v120|, v160
	v_fma_f32 v161, v70, |v124|, v161
	v_fma_f32 v162, v70, |v128|, v162
	v_fma_f32 v163, v70, |v132|, v163
	v_fma_f32 v160, v71, |v121|, v160
	v_fma_f32 v161, v71, |v125|, v161
	v_fma_f32 v162, v71, |v129|, v162
	v_fma_f32 v163, v71, |v133|, v163
	v_fmac_f32_e32 v87, v72, v142
	v_fmac_f32_e32 v87, v73, v143
	v_fma_f32 v160, v72, |v122|, v160
	v_fma_f32 v161, v72, |v126|, v161
	v_fma_f32 v162, v72, |v130|, v162
	v_fma_f32 v163, v72, |v134|, v163
	v_fma_f32 v160, v73, |v123|, v160
	v_fma_f32 v161, v73, |v127|, v161
	v_fma_f32 v162, v73, |v131|, v162
	v_fma_f32 v163, v73, |v135|, v163
	v_add_f32_e32 v104, v34, v144
	v_add_f32_e32 v108, v38, v144
	v_add_f32_e32 v112, v42, v144
	v_add_f32_e32 v116, v46, v144
	v_add_f32_e32 v105, v35, v145
	v_add_f32_e32 v109, v39, v145
	v_add_f32_e32 v113, v43, v145
	v_add_f32_e32 v117, v47, v145
	v_add_f32_e32 v106, v36, v146
	v_add_f32_e32 v110, v40, v146
	v_add_f32_e32 v114, v44, v146
	v_add_f32_e32 v118, v48, v146
	v_add_f32_e32 v107, v37, v147
	v_add_f32_e32 v111, v41, v147
	v_add_f32_e32 v115, v45, v147
	v_add_f32_e32 v119, v49, v147
	v_fmac_f32_e32 v87, v74, v144
	v_fmac_f32_e32 v87, v75, v145
	v_fma_f32 v160, v74, |v104|, v160
	v_fma_f32 v161, v74, |v108|, v161
	v_fma_f32 v162, v74, |v112|, v162
	v_fma_f32 v163, v74, |v116|, v163
	v_fma_f32 v160, v75, |v105|, v160
	v_fma_f32 v161, v75, |v109|, v161
	v_fma_f32 v162, v75, |v113|, v162
	v_fma_f32 v163, v75, |v117|, v163
	v_fmac_f32_e32 v87, v76, v146
	v_fmac_f32_e32 v87, v77, v147
	v_fma_f32 v160, v76, |v106|, v160
	v_fma_f32 v161, v76, |v110|, v161
	v_fma_f32 v162, v76, |v114|, v162
	v_fma_f32 v163, v76, |v118|, v163
	v_fma_f32 v160, v77, |v107|, v160
	v_fma_f32 v161, v77, |v111|, v161
	v_fma_f32 v162, v77, |v115|, v162
	v_fma_f32 v163, v77, |v119|, v163
	v_add_f32_e32 v120, v50, v148
	v_add_f32_e32 v124, v54, v148
	v_add_f32_e32 v128, v58, v148
	v_add_f32_e32 v132, v62, v148
	v_add_f32_e32 v121, v51, v149
	v_add_f32_e32 v125, v55, v149
	v_add_f32_e32 v129, v59, v149
	v_add_f32_e32 v133, v63, v149
	v_add_f32_e32 v122, v52, v150
	v_add_f32_e32 v126, v56, v150
	v_add_f32_e32 v130, v60, v150
	v_add_f32_e32 v134, v64, v150
	v_add_f32_e32 v123, v53, v151
	v_add_f32_e32 v127, v57, v151
	v_add_f32_e32 v131, v61, v151
	v_add_f32_e32 v135, v65, v151
	v_fmac_f32_e32 v87, v78, v148
	v_fmac_f32_e32 v87, v79, v149
	v_fma_f32 v160, v78, |v120|, v160
	v_fma_f32 v161, v78, |v124|, v161
	v_fma_f32 v162, v78, |v128|, v162
	v_fma_f32 v163, v78, |v132|, v163
	v_fma_f32 v160, v79, |v121|, v160
	v_fma_f32 v161, v79, |v125|, v161
	v_fma_f32 v162, v79, |v129|, v162
	v_fma_f32 v163, v79, |v133|, v163
	v_fmac_f32_e32 v87, v80, v150
	v_fmac_f32_e32 v87, v81, v151
	v_fma_f32 v160, v80, |v122|, v160
	v_fma_f32 v161, v80, |v126|, v161
	v_fma_f32 v162, v80, |v130|, v162
	v_fma_f32 v163, v80, |v134|, v163
	v_fma_f32 v160, v81, |v123|, v160
	v_fma_f32 v161, v81, |v127|, v161
	v_fma_f32 v162, v81, |v131|, v162
	v_fma_f32 v163, v81, |v135|, v163
	v_add_f32_e32 v160, v160, v87
	v_add_f32_e32 v161, v161, v87
	v_add_f32_e32 v162, v162, v87
	v_add_f32_e32 v163, v163, v87
	ds_write2_b32 v1, v160, v161 offset1:32
	ds_write2_b32 v1, v162, v163 offset0:64 offset1:96
	v_add_u32_e32 v1, 0x1000, v1
	s_cmpk_eq_i32 s0, 0x1600
	s_cbranch_scc0 .Ltopic_loop
	v_lshl_or_b32 v1, v227, 12, v226
	s_waitcnt lgkmcnt(0)
	s_barrier
	ds_read2st64_b32 v[2:3], v1 offset0:40 offset1:42
	ds_read2st64_b32 v[4:5], v1 offset0:44 offset1:46
	ds_read2st64_b32 v[6:7], v1 offset0:48 offset1:50
	v_or_b32_e32 v13, 16, v227
	s_waitcnt lgkmcnt(2)
	v_add_f32_e32 v2, s18, v2
	v_add_f32_e32 v8, v2, v3
	ds_read2st64_b32 v[2:3], v1 offset0:52 offset1:54
	s_waitcnt lgkmcnt(2)
	v_add_f32_e32 v4, v8, v4
	v_add_f32_e32 v4, v4, v5
	s_waitcnt lgkmcnt(1)
	v_add_f32_e32 v4, v4, v6
	v_add_f32_e32 v4, v4, v7
	s_waitcnt lgkmcnt(0)
	v_add_f32_e32 v2, v4, v2
	v_add_f32_e32 v2, v2, v3
	v_mul_f32_e32 v2, 0xbfb8aa3b, v2
	v_exp_f32_e32 v2, v2
	s_nop 0
	v_add_f32_e32 v4, 1.0, v2
	v_div_scale_f32 v5, s[0:1], v4, v4, 1.0
	v_rcp_f32_e32 v6, v5
	v_div_scale_f32 v7, vcc, 1.0, v4, 1.0
	ds_read2st64_b32 v[2:3], v1 offset0:104 offset1:106
	v_fma_f32 v8, -v5, v6, 1.0
	v_fmac_f32_e32 v6, v8, v6
	v_mul_f32_e32 v8, v7, v6
	v_fma_f32 v9, -v5, v8, v7
	v_fmac_f32_e32 v8, v9, v6
	v_fma_f32 v5, -v5, v8, v7
	v_div_fmas_f32 v5, v5, v6, v8
	v_div_fixup_f32 v8, v5, v4, 1.0
	ds_read2st64_b32 v[4:5], v1 offset0:108 offset1:110
	ds_read2st64_b32 v[6:7], v1 offset0:112 offset1:114
	s_waitcnt lgkmcnt(2)
	v_add_f32_e32 v2, s18, v2
	v_add_f32_e32 v9, v2, v3
	ds_read2st64_b32 v[2:3], v1 offset0:116 offset1:118
	s_waitcnt lgkmcnt(2)
	v_add_f32_e32 v4, v9, v4
	v_add_f32_e32 v4, v4, v5
	s_waitcnt lgkmcnt(1)
	v_add_f32_e32 v4, v4, v6
	v_add_f32_e32 v4, v4, v7
	s_waitcnt lgkmcnt(0)
	v_add_f32_e32 v2, v4, v2
	v_add_f32_e32 v2, v2, v3
	v_mul_f32_e32 v2, 0xbfb8aa3b, v2
	v_exp_f32_e32 v2, v2
	v_lshlrev_b32_e32 v3, 2, v227
	v_or_b32_e32 v6, 8, v227
	v_mov_b32_e32 v7, 0x17000
	v_add_f32_e32 v10, 1.0, v2
	v_div_scale_f32 v5, s[0:1], v10, v10, 1.0
	v_rcp_f32_e32 v11, v5
	v_or_b32_e32 v4, 0x17000, v3
	v_lshl_or_b32 v12, v6, 2, v7
	v_or_b32_e32 v2, 0x17010, v3
	v_or_b32_e32 v3, 0x17030, v3
	v_lshl_or_b32 v7, v13, 2, v7
	ds_read_b32 v4, v4
	ds_read_b32 v14, v2
	ds_read_b32 v12, v12
	ds_read_b32 v15, v3
	ds_read_b32 v16, v7
	s_waitcnt lgkmcnt(4)
	v_fmaak_f32 v2, v8, v4, 0xbc23d70a
	v_max_f32_e32 v8, 0, v2
	v_fma_f32 v2, -v5, v11, 1.0
	v_fmac_f32_e32 v11, v2, v11
	v_div_scale_f32 v4, vcc, 1.0, v10, 1.0
	v_mul_f32_e32 v17, v4, v11
	v_lshl_or_b32 v18, v6, 12, v226
	ds_read2st64_b32 v[2:3], v18 offset0:40 offset1:42
	v_fma_f32 v6, -v5, v17, v4
	v_fmac_f32_e32 v17, v6, v11
	v_fma_f32 v19, -v5, v17, v4
	ds_read2st64_b32 v[4:5], v18 offset0:44 offset1:46
	ds_read2st64_b32 v[6:7], v18 offset0:48 offset1:50
	s_waitcnt lgkmcnt(2)
	v_add_f32_e32 v2, s18, v2
	v_add_f32_e32 v20, v2, v3
	ds_read2st64_b32 v[2:3], v18 offset0:52 offset1:54
	s_waitcnt lgkmcnt(2)
	v_add_f32_e32 v4, v20, v4
	v_add_f32_e32 v4, v4, v5
	s_waitcnt lgkmcnt(1)
	v_add_f32_e32 v4, v4, v6
	v_add_f32_e32 v4, v4, v7
	s_waitcnt lgkmcnt(0)
	v_add_f32_e32 v2, v4, v2
	v_add_f32_e32 v2, v2, v3
	v_mul_f32_e32 v2, 0xbfb8aa3b, v2
	v_exp_f32_e32 v2, v2
	v_div_fmas_f32 v3, v19, v11, v17
	v_div_fixup_f32 v3, v3, v10, 1.0
	v_mov_b32_e32 v9, 0xbc23d70a
	v_add_f32_e32 v10, 1.0, v2
	v_div_scale_f32 v4, s[0:1], v10, v10, 1.0
	v_rcp_f32_e32 v11, v4
	v_fmaak_f32 v2, v3, v14, 0xbc23d70a
	v_max_f32_e32 v2, 0, v2
	v_add_f32_e32 v8, v8, v2
	v_fma_f32 v2, -v4, v11, 1.0
	v_fmac_f32_e32 v11, v2, v11
	v_div_scale_f32 v5, vcc, 1.0, v10, 1.0
	v_mul_f32_e32 v14, v5, v11
	ds_read2st64_b32 v[2:3], v1 offset0:232 offset1:234
	v_fma_f32 v6, -v4, v14, v5
	v_fmac_f32_e32 v14, v6, v11
	v_fma_f32 v17, -v4, v14, v5
	ds_read2st64_b32 v[4:5], v1 offset0:236 offset1:238
	ds_read2st64_b32 v[6:7], v1 offset0:240 offset1:242
	s_waitcnt lgkmcnt(2)
	v_add_f32_e32 v2, s18, v2
	v_add_f32_e32 v18, v2, v3
	ds_read2st64_b32 v[2:3], v1 offset0:244 offset1:246
	s_waitcnt lgkmcnt(2)
	v_add_f32_e32 v1, v18, v4
	v_add_f32_e32 v1, v1, v5
	s_waitcnt lgkmcnt(1)
	v_add_f32_e32 v1, v1, v6
	v_add_f32_e32 v1, v1, v7
	s_waitcnt lgkmcnt(0)
	v_add_f32_e32 v1, v1, v2
	v_add_f32_e32 v1, v1, v3
	v_mul_f32_e32 v1, 0xbfb8aa3b, v1
	v_exp_f32_e32 v1, v1
	v_div_fmas_f32 v2, v17, v11, v14
	v_div_fixup_f32 v2, v2, v10, 1.0
	v_fmaak_f32 v2, v2, v12, 0xbc23d70a
	v_add_f32_e32 v1, 1.0, v1
	v_div_scale_f32 v4, s[0:1], v1, v1, 1.0
	v_rcp_f32_e32 v10, v4
	v_max_f32_e32 v2, 0, v2
	v_add_f32_e32 v8, v8, v2
	v_div_scale_f32 v5, vcc, 1.0, v1, 1.0
	v_fma_f32 v2, -v4, v10, 1.0
	v_fmac_f32_e32 v10, v2, v10
	v_mul_f32_e32 v11, v5, v10
	v_lshl_or_b32 v12, v13, 12, v226
	ds_read2st64_b32 v[2:3], v12 offset0:40 offset1:42
	v_fma_f32 v6, -v4, v11, v5
	v_fmac_f32_e32 v11, v6, v10
	v_fma_f32 v13, -v4, v11, v5
	ds_read2st64_b32 v[4:5], v12 offset0:44 offset1:46
	ds_read2st64_b32 v[6:7], v12 offset0:48 offset1:50
	s_waitcnt lgkmcnt(2)
	v_add_f32_e32 v2, s18, v2
	v_add_f32_e32 v14, v2, v3
	ds_read2st64_b32 v[2:3], v12 offset0:52 offset1:54
	s_waitcnt lgkmcnt(2)
	v_add_f32_e32 v4, v14, v4
	v_add_f32_e32 v4, v4, v5
	s_waitcnt lgkmcnt(1)
	v_add_f32_e32 v4, v4, v6
	v_add_f32_e32 v4, v4, v7
	s_waitcnt lgkmcnt(0)
	v_add_f32_e32 v2, v4, v2
	v_add_f32_e32 v2, v2, v3
	v_mul_f32_e32 v2, 0xbfb8aa3b, v2
	v_exp_f32_e32 v2, v2
	v_div_fmas_f32 v3, v13, v10, v11
	v_div_fixup_f32 v1, v3, v1, 1.0
	v_fmaak_f32 v1, v1, v15, 0xbc23d70a
	v_add_f32_e32 v2, 1.0, v2
	v_div_scale_f32 v3, s[0:1], v2, v2, 1.0
	v_rcp_f32_e32 v4, v3
	v_max_f32_e32 v1, 0, v1
	v_add_f32_e32 v1, v8, v1
	s_lshl_b32 s0, s42, 5
	v_fma_f32 v5, -v3, v4, 1.0
	v_fmac_f32_e32 v4, v5, v4
	v_div_scale_f32 v5, vcc, 1.0, v2, 1.0
	v_mul_f32_e32 v6, v5, v4
	v_fma_f32 v7, -v3, v6, v5
	v_fmac_f32_e32 v6, v7, v4
	v_fma_f32 v3, -v3, v6, v5
	v_div_fmas_f32 v3, v3, v4, v6
	v_div_fixup_f32 v2, v3, v2, 1.0
	v_fmac_f32_e32 v9, v2, v16
	v_max_f32_e32 v2, 0, v9
	v_add_f32_e32 v2, v1, v2
	v_mov_b32_e32 v1, 0x16800
	v_lshl_or_b32 v1, v0, 2, v1
	v_cmp_gt_u32_e32 vcc, s0, v0
	ds_write_b32 v1, v2
	s_waitcnt lgkmcnt(0)
	s_barrier
	s_and_saveexec_b64 s[0:1], vcc
	s_cbranch_execz .LBB1_57
	ds_read2st64_b32 v[2:3], v1 offset1:2
	ds_read2st64_b32 v[4:5], v1 offset0:4 offset1:6
	v_add_u32_e32 v0, s33, v0
	v_ashrrev_i32_e32 v1, 31, v0
	v_lshl_add_u64 v[6:7], v[0:1], 2, s[10:11]
	s_waitcnt lgkmcnt(1)
	v_add_f32_e32 v1, v2, v3
	s_waitcnt lgkmcnt(0)
	v_add_f32_e32 v1, v1, v4
	v_add_f32_e32 v1, v1, v5
	v_add_u32_e32 v0, 0x7d00, v0
	v_mul_f32_e32 v2, 0x3d4ccccd, v1
	v_ashrrev_i32_e32 v1, 31, v0
	v_lshl_add_u64 v[0:1], v[0:1], 2, s[10:11]
	global_store_dword v[6:7], v2, off
	global_store_dword v[0:1], v2, off
